# P5 projection epilogue: merge-gate loads issued up front with counted waits (+2 wait states after 128-bit stores)
# baseline (speedup 1.0000x reference)
.LBB0_1006:
	v_lshl_add_u32 v136, s34, 8, v1
	s_lshl_b32 s27, s35, 8
	v_or_b32_e32 v140, s27, v175
	v_or_b32_e32 v134, 16, v136
	v_or_b32_e32 v138, 32, v136
	v_or_b32_e32 v4, 48, v136
	s_cmp_eq_u32 s59, 0
	v_ashrrev_i32_e32 v141, 31, v140
	v_ashrrev_i32_e32 v137, 31, v136
	v_ashrrev_i32_e32 v135, 31, v134
	v_ashrrev_i32_e32 v139, 31, v138
	v_ashrrev_i32_e32 v5, 31, v4
	s_cbranch_scc1 .LBB0_1008
	v_lshl_add_u32 v195, v136, 12, v140
	global_load_dwordx4 v[196:199], v195, s[12:13] offset:2048
	v_add_u32_e32 v220, 0x10000, v195
	global_load_dwordx4 v[200:203], v220, s[12:13] offset:2048
	v_add_u32_e32 v220, 0x20000, v195
	global_load_dwordx4 v[204:207], v220, s[12:13] offset:2048
	v_add_u32_e32 v220, 0x30000, v195
	global_load_dwordx4 v[208:211], v220, s[12:13] offset:2048
	v_add_u32_e32 v220, 0x80000, v195
	global_load_dwordx4 v[212:215], v220, s[12:13] offset:2048
	v_add_u32_e32 v220, 0x90000, v195
	global_load_dwordx4 v[216:219], v220, s[12:13] offset:2048
	v_lshlrev_b64 v[142:143], 12, v[136:137]
	v_lshl_add_u64 v[144:145], s[12:13], 0, v[142:143]
	v_lshl_add_u64 v[144:145], v[144:145], 0, v[140:141]
	v_or_b32_e32 v144, s27, v176
	v_lshlrev_b64 v[178:179], 12, v[134:135]
	v_ashrrev_i32_e32 v145, 31, v144
	v_lshl_add_u64 v[170:171], s[14:15], 0, v[142:143]
	v_lshl_add_u64 v[172:173], s[12:13], 0, v[178:179]
	v_lshlrev_b64 v[144:145], 1, v[144:145]
	v_lshl_add_u64 v[180:181], v[172:173], 0, v[140:141]
	v_lshl_add_u64 v[182:183], v[170:171], 0, v[144:145]
	s_mov_b64 s[34:35], 0
	s_waitcnt vmcnt(5)
	v_cvt_f32_ubyte0_e32 v3, v196
	v_cvt_f32_ubyte0_e32 v170, v197
	v_cvt_f32_ubyte1_e32 v171, v196
	v_cvt_f32_ubyte1_e32 v172, v197
	v_cvt_f32_ubyte2_e32 v173, v196
	v_cvt_f32_ubyte2_e32 v184, v197
	v_cvt_f32_ubyte3_e32 v185, v196
	v_cvt_f32_ubyte3_e32 v186, v197
	v_cvt_f32_ubyte0_e32 v187, v198
	v_cvt_f32_ubyte0_e32 v188, v199
	v_cvt_f32_ubyte1_e32 v189, v198
	v_cvt_f32_ubyte1_e32 v190, v199
	v_cvt_f32_ubyte2_e32 v191, v198
	v_cvt_f32_ubyte2_e32 v192, v199
	v_cvt_f32_ubyte3_e32 v193, v198
	v_cvt_f32_ubyte3_e32 v194, v199
	v_max_f32_e32 v146, 0.5, v3
	v_max_f32_e32 v148, 0.5, v170
	v_max_f32_e32 v147, 0.5, v171
	v_max_f32_e32 v149, 0.5, v172
	v_max_f32_e32 v170, 0.5, v173
	v_max_f32_e32 v172, 0.5, v184
	v_max_f32_e32 v171, 0.5, v185
	v_max_f32_e32 v173, 0.5, v186
	v_max_f32_e32 v184, 0.5, v187
	v_max_f32_e32 v186, 0.5, v188
	v_max_f32_e32 v185, 0.5, v189
	v_max_f32_e32 v187, 0.5, v190
	v_max_f32_e32 v188, 0.5, v191
	v_max_f32_e32 v190, 0.5, v192
	v_max_f32_e32 v189, 0.5, v193
	v_max_f32_e32 v191, 0.5, v194
	v_pk_mul_f32 v[146:147], v[146:147], s[16:17] op_sel_hi:[1,0]
	v_pk_mul_f32 v[148:149], v[148:149], s[16:17] op_sel_hi:[1,0]
	v_pk_mul_f32 v[170:171], v[170:171], s[16:17] op_sel_hi:[1,0]
	v_pk_mul_f32 v[172:173], v[172:173], s[16:17] op_sel_hi:[1,0]
	v_pk_mul_f32 v[184:185], v[184:185], s[16:17] op_sel_hi:[1,0]
	v_pk_mul_f32 v[186:187], v[186:187], s[16:17] op_sel_hi:[1,0]
	v_pk_mul_f32 v[188:189], v[188:189], s[16:17] op_sel_hi:[1,0]
	v_pk_mul_f32 v[190:191], v[190:191], s[16:17] op_sel_hi:[1,0]
	v_pk_mul_f32 v[146:147], v[98:99], v[146:147]
	v_pk_mul_f32 v[148:149], v[94:95], v[148:149]
	v_pk_mul_f32 v[170:171], v[100:101], v[170:171]
	v_pk_mul_f32 v[172:173], v[96:97], v[172:173]
	v_pk_mul_f32 v[184:185], v[66:67], v[184:185]
	v_pk_mul_f32 v[186:187], v[62:63], v[186:187]
	v_pk_mul_f32 v[188:189], v[68:69], v[188:189]
	v_pk_mul_f32 v[190:191], v[64:65], v[190:191]
	v_cvt_pk_bf16_f32 v146, v146, v147
	v_cvt_pk_bf16_f32 v147, v170, v171
	v_cvt_pk_bf16_f32 v148, v148, v149
	v_cvt_pk_bf16_f32 v149, v172, v173
	v_cvt_pk_bf16_f32 v170, v184, v185
	v_cvt_pk_bf16_f32 v171, v188, v189
	v_cvt_pk_bf16_f32 v172, v186, v187
	v_cvt_pk_bf16_f32 v173, v190, v191
	global_store_dwordx4 v[182:183], v[146:149], off
	global_store_dwordx4 v[182:183], v[170:173], off offset:256
	v_add_u32_e32 v220, 0xa0000, v195
	global_load_dwordx4 v[196:199], v220, s[12:13] offset:2048
	v_lshlrev_b64 v[180:181], 12, v[138:139]
	v_lshl_add_u64 v[170:171], s[14:15], 0, v[178:179]
	v_lshl_add_u64 v[172:173], s[12:13], 0, v[180:181]
	v_lshl_add_u64 v[178:179], v[172:173], 0, v[140:141]
	v_lshl_add_u64 v[182:183], v[170:171], 0, v[144:145]
	s_waitcnt vmcnt(7)
	v_cvt_f32_ubyte0_e32 v3, v200
	v_cvt_f32_ubyte0_e32 v170, v201
	v_cvt_f32_ubyte1_e32 v171, v200
	v_cvt_f32_ubyte1_e32 v172, v201
	v_cvt_f32_ubyte2_e32 v173, v200
	v_cvt_f32_ubyte2_e32 v184, v201
	v_cvt_f32_ubyte3_e32 v185, v200
	v_cvt_f32_ubyte3_e32 v186, v201
	v_cvt_f32_ubyte0_e32 v187, v202
	v_cvt_f32_ubyte0_e32 v188, v203
	v_cvt_f32_ubyte1_e32 v189, v202
	v_cvt_f32_ubyte1_e32 v190, v203
	v_cvt_f32_ubyte2_e32 v191, v202
	v_cvt_f32_ubyte2_e32 v192, v203
	v_cvt_f32_ubyte3_e32 v193, v202
	v_cvt_f32_ubyte3_e32 v194, v203
	v_max_f32_e32 v146, 0.5, v3
	v_max_f32_e32 v148, 0.5, v170
	v_max_f32_e32 v147, 0.5, v171
	v_max_f32_e32 v149, 0.5, v172
	v_max_f32_e32 v170, 0.5, v173
	v_max_f32_e32 v172, 0.5, v184
	v_max_f32_e32 v171, 0.5, v185
	v_max_f32_e32 v173, 0.5, v186
	v_max_f32_e32 v184, 0.5, v187
	v_max_f32_e32 v186, 0.5, v188
	v_max_f32_e32 v185, 0.5, v189
	v_max_f32_e32 v187, 0.5, v190
	v_max_f32_e32 v188, 0.5, v191
	v_max_f32_e32 v190, 0.5, v192
	v_max_f32_e32 v189, 0.5, v193
	v_max_f32_e32 v191, 0.5, v194
	v_pk_mul_f32 v[146:147], v[146:147], s[16:17] op_sel_hi:[1,0]
	v_pk_mul_f32 v[148:149], v[148:149], s[16:17] op_sel_hi:[1,0]
	v_pk_mul_f32 v[170:171], v[170:171], s[16:17] op_sel_hi:[1,0]
	v_pk_mul_f32 v[172:173], v[172:173], s[16:17] op_sel_hi:[1,0]
	v_pk_mul_f32 v[184:185], v[184:185], s[16:17] op_sel_hi:[1,0]
	v_pk_mul_f32 v[186:187], v[186:187], s[16:17] op_sel_hi:[1,0]
	v_pk_mul_f32 v[188:189], v[188:189], s[16:17] op_sel_hi:[1,0]
	v_pk_mul_f32 v[190:191], v[190:191], s[16:17] op_sel_hi:[1,0]
	v_pk_mul_f32 v[146:147], v[90:91], v[146:147]
	v_pk_mul_f32 v[148:149], v[86:87], v[148:149]
	v_pk_mul_f32 v[170:171], v[92:93], v[170:171]
	v_pk_mul_f32 v[172:173], v[88:89], v[172:173]
	v_pk_mul_f32 v[184:185], v[58:59], v[184:185]
	v_pk_mul_f32 v[186:187], v[54:55], v[186:187]
	v_pk_mul_f32 v[188:189], v[60:61], v[188:189]
	v_pk_mul_f32 v[190:191], v[56:57], v[190:191]
	v_cvt_pk_bf16_f32 v146, v146, v147
	v_cvt_pk_bf16_f32 v147, v170, v171
	v_cvt_pk_bf16_f32 v148, v148, v149
	v_cvt_pk_bf16_f32 v149, v172, v173
	v_cvt_pk_bf16_f32 v170, v184, v185
	v_cvt_pk_bf16_f32 v171, v188, v189
	v_cvt_pk_bf16_f32 v172, v186, v187
	v_cvt_pk_bf16_f32 v173, v190, v191
	global_store_dwordx4 v[182:183], v[146:149], off
	global_store_dwordx4 v[182:183], v[170:173], off offset:256
	v_add_u32_e32 v220, 0xb0000, v195
	global_load_dwordx4 v[200:203], v220, s[12:13] offset:2048
	v_lshlrev_b64 v[178:179], 12, v[4:5]
	v_lshl_add_u64 v[170:171], s[14:15], 0, v[180:181]
	v_lshl_add_u64 v[172:173], s[12:13], 0, v[178:179]
	v_lshl_add_u64 v[180:181], v[172:173], 0, v[140:141]
	v_lshl_add_u64 v[182:183], v[170:171], 0, v[144:145]
	s_waitcnt vmcnt(9)
	v_cvt_f32_ubyte0_e32 v3, v204
	v_cvt_f32_ubyte0_e32 v170, v205
	v_cvt_f32_ubyte1_e32 v171, v204
	v_cvt_f32_ubyte1_e32 v172, v205
	v_cvt_f32_ubyte2_e32 v173, v204
	v_cvt_f32_ubyte2_e32 v184, v205
	v_cvt_f32_ubyte3_e32 v185, v204
	v_cvt_f32_ubyte3_e32 v186, v205
	v_cvt_f32_ubyte0_e32 v187, v206
	v_cvt_f32_ubyte0_e32 v188, v207
	v_cvt_f32_ubyte1_e32 v189, v206
	v_cvt_f32_ubyte1_e32 v190, v207
	v_cvt_f32_ubyte2_e32 v191, v206
	v_cvt_f32_ubyte2_e32 v192, v207
	v_cvt_f32_ubyte3_e32 v193, v206
	v_cvt_f32_ubyte3_e32 v194, v207
	v_max_f32_e32 v146, 0.5, v3
	v_max_f32_e32 v148, 0.5, v170
	v_max_f32_e32 v147, 0.5, v171
	v_max_f32_e32 v149, 0.5, v172
	v_max_f32_e32 v170, 0.5, v173
	v_max_f32_e32 v172, 0.5, v184
	v_max_f32_e32 v171, 0.5, v185
	v_max_f32_e32 v173, 0.5, v186
	v_max_f32_e32 v184, 0.5, v187
	v_max_f32_e32 v186, 0.5, v188
	v_max_f32_e32 v185, 0.5, v189
	v_max_f32_e32 v187, 0.5, v190
	v_max_f32_e32 v188, 0.5, v191
	v_max_f32_e32 v190, 0.5, v192
	v_max_f32_e32 v189, 0.5, v193
	v_max_f32_e32 v191, 0.5, v194
	v_pk_mul_f32 v[146:147], v[146:147], s[16:17] op_sel_hi:[1,0]
	v_pk_mul_f32 v[148:149], v[148:149], s[16:17] op_sel_hi:[1,0]
	v_pk_mul_f32 v[170:171], v[170:171], s[16:17] op_sel_hi:[1,0]
	v_pk_mul_f32 v[172:173], v[172:173], s[16:17] op_sel_hi:[1,0]
	v_pk_mul_f32 v[184:185], v[184:185], s[16:17] op_sel_hi:[1,0]
	v_pk_mul_f32 v[186:187], v[186:187], s[16:17] op_sel_hi:[1,0]
	v_pk_mul_f32 v[188:189], v[188:189], s[16:17] op_sel_hi:[1,0]
	v_pk_mul_f32 v[190:191], v[190:191], s[16:17] op_sel_hi:[1,0]
	v_pk_mul_f32 v[146:147], v[82:83], v[146:147]
	v_pk_mul_f32 v[148:149], v[78:79], v[148:149]
	v_pk_mul_f32 v[170:171], v[84:85], v[170:171]
	v_pk_mul_f32 v[172:173], v[80:81], v[172:173]
	v_pk_mul_f32 v[184:185], v[50:51], v[184:185]
	v_pk_mul_f32 v[186:187], v[46:47], v[186:187]
	v_pk_mul_f32 v[188:189], v[52:53], v[188:189]
	v_pk_mul_f32 v[190:191], v[48:49], v[190:191]
	v_cvt_pk_bf16_f32 v146, v146, v147
	v_cvt_pk_bf16_f32 v147, v170, v171
	v_cvt_pk_bf16_f32 v148, v148, v149
	v_cvt_pk_bf16_f32 v149, v172, v173
	v_cvt_pk_bf16_f32 v170, v184, v185
	v_cvt_pk_bf16_f32 v171, v188, v189
	v_cvt_pk_bf16_f32 v172, v186, v187
	v_cvt_pk_bf16_f32 v173, v190, v191
	global_store_dwordx4 v[182:183], v[146:149], off
	global_store_dwordx4 v[182:183], v[170:173], off offset:256
	s_nop 1
	s_waitcnt vmcnt(10)
	v_cvt_f32_ubyte0_e32 v3, v208
	v_lshl_add_u64 v[170:171], s[14:15], 0, v[178:179]
	v_lshl_add_u64 v[178:179], v[142:143], 0, s[0:1]
	v_lshl_add_u64 v[172:173], s[12:13], 0, v[178:179]
	v_lshl_add_u64 v[180:181], v[170:171], 0, v[144:145]
	v_lshl_add_u64 v[182:183], v[172:173], 0, v[140:141]
	v_cvt_f32_ubyte0_e32 v170, v209
	v_cvt_f32_ubyte1_e32 v171, v208
	v_cvt_f32_ubyte1_e32 v172, v209
	v_cvt_f32_ubyte2_e32 v173, v208
	v_cvt_f32_ubyte2_e32 v184, v209
	v_cvt_f32_ubyte3_e32 v185, v208
	v_cvt_f32_ubyte3_e32 v186, v209
	v_cvt_f32_ubyte0_e32 v187, v210
	v_cvt_f32_ubyte0_e32 v188, v211
	v_cvt_f32_ubyte1_e32 v189, v210
	v_cvt_f32_ubyte1_e32 v190, v211
	v_cvt_f32_ubyte2_e32 v191, v210
	v_cvt_f32_ubyte2_e32 v192, v211
	v_cvt_f32_ubyte3_e32 v193, v210
	v_cvt_f32_ubyte3_e32 v194, v211
	v_max_f32_e32 v146, 0.5, v3
	v_max_f32_e32 v148, 0.5, v170
	v_max_f32_e32 v147, 0.5, v171
	v_max_f32_e32 v149, 0.5, v172
	v_max_f32_e32 v170, 0.5, v173
	v_max_f32_e32 v172, 0.5, v184
	v_max_f32_e32 v171, 0.5, v185
	v_max_f32_e32 v173, 0.5, v186
	v_max_f32_e32 v184, 0.5, v187
	v_max_f32_e32 v186, 0.5, v188
	v_max_f32_e32 v185, 0.5, v189
	v_max_f32_e32 v187, 0.5, v190
	v_max_f32_e32 v188, 0.5, v191
	v_max_f32_e32 v190, 0.5, v192
	v_max_f32_e32 v189, 0.5, v193
	v_max_f32_e32 v191, 0.5, v194
	v_pk_mul_f32 v[146:147], v[146:147], s[16:17] op_sel_hi:[1,0]
	v_pk_mul_f32 v[148:149], v[148:149], s[16:17] op_sel_hi:[1,0]
	v_pk_mul_f32 v[170:171], v[170:171], s[16:17] op_sel_hi:[1,0]
	v_pk_mul_f32 v[172:173], v[172:173], s[16:17] op_sel_hi:[1,0]
	v_pk_mul_f32 v[184:185], v[184:185], s[16:17] op_sel_hi:[1,0]
	v_pk_mul_f32 v[186:187], v[186:187], s[16:17] op_sel_hi:[1,0]
	v_pk_mul_f32 v[188:189], v[188:189], s[16:17] op_sel_hi:[1,0]
	v_pk_mul_f32 v[190:191], v[190:191], s[16:17] op_sel_hi:[1,0]
	v_pk_mul_f32 v[146:147], v[74:75], v[146:147]
	v_pk_mul_f32 v[148:149], v[70:71], v[148:149]
	v_pk_mul_f32 v[170:171], v[76:77], v[170:171]
	v_pk_mul_f32 v[172:173], v[72:73], v[172:173]
	v_pk_mul_f32 v[184:185], v[42:43], v[184:185]
	v_pk_mul_f32 v[186:187], v[38:39], v[186:187]
	v_pk_mul_f32 v[188:189], v[44:45], v[188:189]
	v_pk_mul_f32 v[190:191], v[40:41], v[190:191]
	v_cvt_pk_bf16_f32 v146, v146, v147
	v_cvt_pk_bf16_f32 v147, v170, v171
	v_cvt_pk_bf16_f32 v148, v148, v149
	v_cvt_pk_bf16_f32 v149, v172, v173
	v_cvt_pk_bf16_f32 v170, v184, v185
	v_cvt_pk_bf16_f32 v171, v188, v189
	v_cvt_pk_bf16_f32 v172, v186, v187
	v_cvt_pk_bf16_f32 v173, v190, v191
	global_store_dwordx4 v[180:181], v[146:149], off
	global_store_dwordx4 v[180:181], v[170:173], off offset:256
	s_nop 1
	v_lshl_add_u64 v[180:181], v[142:143], 0, s[18:19]
	v_lshl_add_u64 v[170:171], s[14:15], 0, v[178:179]
	v_lshl_add_u64 v[172:173], s[12:13], 0, v[180:181]
	v_lshl_add_u64 v[178:179], v[170:171], 0, v[144:145]
	v_lshl_add_u64 v[182:183], v[172:173], 0, v[140:141]
	s_waitcnt vmcnt(11)
	v_cvt_f32_ubyte0_e32 v3, v212
	v_cvt_f32_ubyte0_e32 v170, v213
	v_cvt_f32_ubyte1_e32 v171, v212
	v_cvt_f32_ubyte1_e32 v172, v213
	v_cvt_f32_ubyte2_e32 v173, v212
	v_cvt_f32_ubyte2_e32 v184, v213
	v_cvt_f32_ubyte3_e32 v185, v212
	v_cvt_f32_ubyte3_e32 v186, v213
	v_cvt_f32_ubyte0_e32 v187, v214
	v_cvt_f32_ubyte0_e32 v188, v215
	v_cvt_f32_ubyte1_e32 v189, v214
	v_cvt_f32_ubyte1_e32 v190, v215
	v_cvt_f32_ubyte2_e32 v191, v214
	v_cvt_f32_ubyte2_e32 v192, v215
	v_cvt_f32_ubyte3_e32 v193, v214
	v_cvt_f32_ubyte3_e32 v194, v215
	v_max_f32_e32 v146, 0.5, v3
	v_max_f32_e32 v148, 0.5, v170
	v_max_f32_e32 v147, 0.5, v171
	v_max_f32_e32 v149, 0.5, v172
	v_max_f32_e32 v170, 0.5, v173
	v_max_f32_e32 v172, 0.5, v184
	v_max_f32_e32 v171, 0.5, v185
	v_max_f32_e32 v173, 0.5, v186
	v_max_f32_e32 v184, 0.5, v187
	v_max_f32_e32 v186, 0.5, v188
	v_max_f32_e32 v185, 0.5, v189
	v_max_f32_e32 v187, 0.5, v190
	v_max_f32_e32 v188, 0.5, v191
	v_max_f32_e32 v190, 0.5, v192
	v_max_f32_e32 v189, 0.5, v193
	v_max_f32_e32 v191, 0.5, v194
	v_pk_mul_f32 v[146:147], v[146:147], s[16:17] op_sel_hi:[1,0]
	v_pk_mul_f32 v[148:149], v[148:149], s[16:17] op_sel_hi:[1,0]
	v_pk_mul_f32 v[170:171], v[170:171], s[16:17] op_sel_hi:[1,0]
	v_pk_mul_f32 v[172:173], v[172:173], s[16:17] op_sel_hi:[1,0]
	v_pk_mul_f32 v[184:185], v[184:185], s[16:17] op_sel_hi:[1,0]
	v_pk_mul_f32 v[186:187], v[186:187], s[16:17] op_sel_hi:[1,0]
	v_pk_mul_f32 v[188:189], v[188:189], s[16:17] op_sel_hi:[1,0]
	v_pk_mul_f32 v[190:191], v[190:191], s[16:17] op_sel_hi:[1,0]
	v_pk_mul_f32 v[146:147], v[34:35], v[146:147]
	v_pk_mul_f32 v[148:149], v[30:31], v[148:149]
	v_pk_mul_f32 v[170:171], v[36:37], v[170:171]
	v_pk_mul_f32 v[172:173], v[32:33], v[172:173]
	v_pk_mul_f32 v[184:185], v[102:103], v[184:185]
	v_pk_mul_f32 v[186:187], v[106:107], v[186:187]
	v_pk_mul_f32 v[188:189], v[104:105], v[188:189]
	v_pk_mul_f32 v[190:191], v[108:109], v[190:191]
	v_cvt_pk_bf16_f32 v146, v146, v147
	v_cvt_pk_bf16_f32 v147, v170, v171
	v_cvt_pk_bf16_f32 v148, v148, v149
	v_cvt_pk_bf16_f32 v149, v172, v173
	v_cvt_pk_bf16_f32 v170, v184, v185
	v_cvt_pk_bf16_f32 v171, v188, v189
	v_cvt_pk_bf16_f32 v172, v186, v187
	v_cvt_pk_bf16_f32 v173, v190, v191
	global_store_dwordx4 v[178:179], v[146:149], off
	global_store_dwordx4 v[178:179], v[170:173], off offset:256
	s_nop 1
	v_lshl_add_u64 v[178:179], v[142:143], 0, s[20:21]
	v_lshl_add_u64 v[170:171], s[14:15], 0, v[180:181]
	v_lshl_add_u64 v[172:173], s[12:13], 0, v[178:179]
	v_lshl_add_u64 v[180:181], v[170:171], 0, v[144:145]
	v_lshl_add_u64 v[182:183], v[172:173], 0, v[140:141]
	v_lshl_add_u64 v[142:143], v[142:143], 0, s[22:23]
	s_waitcnt vmcnt(12)
	v_cvt_f32_ubyte0_e32 v3, v216
	v_cvt_f32_ubyte0_e32 v170, v217
	v_cvt_f32_ubyte1_e32 v171, v216
	v_cvt_f32_ubyte1_e32 v172, v217
	v_cvt_f32_ubyte2_e32 v173, v216
	v_cvt_f32_ubyte2_e32 v184, v217
	v_cvt_f32_ubyte3_e32 v185, v216
	v_cvt_f32_ubyte3_e32 v186, v217
	v_cvt_f32_ubyte0_e32 v187, v218
	v_cvt_f32_ubyte0_e32 v188, v219
	v_cvt_f32_ubyte1_e32 v189, v218
	v_cvt_f32_ubyte1_e32 v190, v219
	v_cvt_f32_ubyte2_e32 v191, v218
	v_cvt_f32_ubyte2_e32 v192, v219
	v_cvt_f32_ubyte3_e32 v193, v218
	v_cvt_f32_ubyte3_e32 v194, v219
	v_max_f32_e32 v146, 0.5, v3
	v_max_f32_e32 v148, 0.5, v170
	v_max_f32_e32 v147, 0.5, v171
	v_max_f32_e32 v149, 0.5, v172
	v_max_f32_e32 v170, 0.5, v173
	v_max_f32_e32 v172, 0.5, v184
	v_max_f32_e32 v171, 0.5, v185
	v_max_f32_e32 v173, 0.5, v186
	v_max_f32_e32 v184, 0.5, v187
	v_max_f32_e32 v186, 0.5, v188
	v_max_f32_e32 v185, 0.5, v189
	v_max_f32_e32 v187, 0.5, v190
	v_max_f32_e32 v188, 0.5, v191
	v_max_f32_e32 v190, 0.5, v192
	v_max_f32_e32 v189, 0.5, v193
	v_max_f32_e32 v191, 0.5, v194
	v_pk_mul_f32 v[146:147], v[146:147], s[16:17] op_sel_hi:[1,0]
	v_pk_mul_f32 v[148:149], v[148:149], s[16:17] op_sel_hi:[1,0]
	v_pk_mul_f32 v[170:171], v[170:171], s[16:17] op_sel_hi:[1,0]
	v_pk_mul_f32 v[172:173], v[172:173], s[16:17] op_sel_hi:[1,0]
	v_pk_mul_f32 v[184:185], v[184:185], s[16:17] op_sel_hi:[1,0]
	v_pk_mul_f32 v[186:187], v[186:187], s[16:17] op_sel_hi:[1,0]
	v_pk_mul_f32 v[188:189], v[188:189], s[16:17] op_sel_hi:[1,0]
	v_pk_mul_f32 v[190:191], v[190:191], s[16:17] op_sel_hi:[1,0]
	v_pk_mul_f32 v[146:147], v[26:27], v[146:147]
	v_pk_mul_f32 v[148:149], v[22:23], v[148:149]
	v_pk_mul_f32 v[170:171], v[28:29], v[170:171]
	v_pk_mul_f32 v[172:173], v[24:25], v[172:173]
	v_pk_mul_f32 v[184:185], v[110:111], v[184:185]
	v_pk_mul_f32 v[186:187], v[114:115], v[186:187]
	v_pk_mul_f32 v[188:189], v[112:113], v[188:189]
	v_pk_mul_f32 v[190:191], v[116:117], v[190:191]
	v_cvt_pk_bf16_f32 v146, v146, v147
	v_cvt_pk_bf16_f32 v147, v170, v171
	v_cvt_pk_bf16_f32 v148, v148, v149
	v_cvt_pk_bf16_f32 v149, v172, v173
	v_cvt_pk_bf16_f32 v170, v184, v185
	v_cvt_pk_bf16_f32 v171, v188, v189
	v_cvt_pk_bf16_f32 v172, v186, v187
	v_cvt_pk_bf16_f32 v173, v190, v191
	global_store_dwordx4 v[180:181], v[146:149], off
	global_store_dwordx4 v[180:181], v[170:173], off offset:256
	s_nop 1
	s_waitcnt vmcnt(11)
	v_cvt_f32_ubyte0_e32 v3, v196
	v_lshl_add_u64 v[170:171], s[14:15], 0, v[178:179]
	v_lshl_add_u64 v[172:173], s[12:13], 0, v[142:143]
	v_lshl_add_u64 v[178:179], v[170:171], 0, v[144:145]
	v_lshl_add_u64 v[180:181], v[172:173], 0, v[140:141]
	v_cvt_f32_ubyte0_e32 v170, v197
	v_cvt_f32_ubyte1_e32 v171, v196
	v_cvt_f32_ubyte1_e32 v172, v197
	v_cvt_f32_ubyte2_e32 v173, v196
	v_cvt_f32_ubyte2_e32 v182, v197
	v_cvt_f32_ubyte3_e32 v183, v196
	v_cvt_f32_ubyte3_e32 v184, v197
	v_cvt_f32_ubyte0_e32 v185, v198
	v_cvt_f32_ubyte0_e32 v186, v199
	v_cvt_f32_ubyte1_e32 v187, v198
	v_cvt_f32_ubyte1_e32 v188, v199
	v_cvt_f32_ubyte2_e32 v189, v198
	v_cvt_f32_ubyte2_e32 v190, v199
	v_cvt_f32_ubyte3_e32 v191, v198
	v_cvt_f32_ubyte3_e32 v192, v199
	v_max_f32_e32 v146, 0.5, v3
	v_max_f32_e32 v148, 0.5, v170
	v_max_f32_e32 v147, 0.5, v171
	v_max_f32_e32 v149, 0.5, v172
	v_max_f32_e32 v170, 0.5, v173
	v_max_f32_e32 v172, 0.5, v182
	v_max_f32_e32 v171, 0.5, v183
	v_max_f32_e32 v173, 0.5, v184
	v_max_f32_e32 v182, 0.5, v185
	v_max_f32_e32 v184, 0.5, v186
	v_max_f32_e32 v183, 0.5, v187
	v_max_f32_e32 v185, 0.5, v188
	v_max_f32_e32 v186, 0.5, v189
	v_max_f32_e32 v188, 0.5, v190
	v_max_f32_e32 v187, 0.5, v191
	v_max_f32_e32 v189, 0.5, v192
	v_pk_mul_f32 v[146:147], v[146:147], s[16:17] op_sel_hi:[1,0]
	v_pk_mul_f32 v[148:149], v[148:149], s[16:17] op_sel_hi:[1,0]
	v_pk_mul_f32 v[170:171], v[170:171], s[16:17] op_sel_hi:[1,0]
	v_pk_mul_f32 v[172:173], v[172:173], s[16:17] op_sel_hi:[1,0]
	v_pk_mul_f32 v[182:183], v[182:183], s[16:17] op_sel_hi:[1,0]
	v_pk_mul_f32 v[184:185], v[184:185], s[16:17] op_sel_hi:[1,0]
	v_pk_mul_f32 v[186:187], v[186:187], s[16:17] op_sel_hi:[1,0]
	v_pk_mul_f32 v[188:189], v[188:189], s[16:17] op_sel_hi:[1,0]
	v_pk_mul_f32 v[146:147], v[18:19], v[146:147]
	v_pk_mul_f32 v[148:149], v[14:15], v[148:149]
	v_pk_mul_f32 v[170:171], v[20:21], v[170:171]
	v_pk_mul_f32 v[172:173], v[16:17], v[172:173]
	v_pk_mul_f32 v[182:183], v[118:119], v[182:183]
	v_pk_mul_f32 v[184:185], v[122:123], v[184:185]
	v_pk_mul_f32 v[186:187], v[120:121], v[186:187]
	v_pk_mul_f32 v[188:189], v[124:125], v[188:189]
	v_cvt_pk_bf16_f32 v146, v146, v147
	v_cvt_pk_bf16_f32 v147, v170, v171
	v_cvt_pk_bf16_f32 v148, v148, v149
	v_cvt_pk_bf16_f32 v149, v172, v173
	v_cvt_pk_bf16_f32 v170, v182, v183
	v_cvt_pk_bf16_f32 v171, v186, v187
	v_cvt_pk_bf16_f32 v172, v184, v185
	v_cvt_pk_bf16_f32 v173, v188, v189
	global_store_dwordx4 v[178:179], v[146:149], off
	global_store_dwordx4 v[178:179], v[170:173], off offset:256
	s_nop 1
	v_lshl_add_u64 v[142:143], s[14:15], 0, v[142:143]
	v_lshl_add_u64 v[170:171], v[142:143], 0, v[144:145]
	s_waitcnt vmcnt(10)
	v_cvt_f32_ubyte0_e32 v3, v200
	v_cvt_f32_ubyte0_e32 v143, v201
	v_cvt_f32_ubyte1_e32 v145, v200
	v_cvt_f32_ubyte1_e32 v172, v201
	v_cvt_f32_ubyte2_e32 v173, v200
	v_cvt_f32_ubyte2_e32 v178, v201
	v_cvt_f32_ubyte3_e32 v179, v200
	v_cvt_f32_ubyte3_e32 v180, v201
	v_cvt_f32_ubyte0_e32 v181, v202
	v_cvt_f32_ubyte0_e32 v182, v203
	v_cvt_f32_ubyte1_e32 v183, v202
	v_cvt_f32_ubyte1_e32 v184, v203
	v_cvt_f32_ubyte2_e32 v185, v202
	v_cvt_f32_ubyte2_e32 v186, v203
	v_cvt_f32_ubyte3_e32 v187, v202
	v_cvt_f32_ubyte3_e32 v188, v203
	v_max_f32_e32 v142, 0.5, v3
	v_max_f32_e32 v144, 0.5, v143
	v_max_f32_e32 v143, 0.5, v145
	v_max_f32_e32 v145, 0.5, v172
	v_max_f32_e32 v146, 0.5, v173
	v_max_f32_e32 v148, 0.5, v178
	v_max_f32_e32 v147, 0.5, v179
	v_max_f32_e32 v149, 0.5, v180
	v_max_f32_e32 v172, 0.5, v181
	v_max_f32_e32 v178, 0.5, v182
	v_max_f32_e32 v173, 0.5, v183
	v_max_f32_e32 v179, 0.5, v184
	v_max_f32_e32 v180, 0.5, v185
	v_max_f32_e32 v182, 0.5, v186
	v_max_f32_e32 v181, 0.5, v187
	v_max_f32_e32 v183, 0.5, v188
	v_pk_mul_f32 v[142:143], v[142:143], s[16:17] op_sel_hi:[1,0]
	v_pk_mul_f32 v[144:145], v[144:145], s[16:17] op_sel_hi:[1,0]
	v_pk_mul_f32 v[146:147], v[146:147], s[16:17] op_sel_hi:[1,0]
	v_pk_mul_f32 v[148:149], v[148:149], s[16:17] op_sel_hi:[1,0]
	v_pk_mul_f32 v[172:173], v[172:173], s[16:17] op_sel_hi:[1,0]
	v_pk_mul_f32 v[178:179], v[178:179], s[16:17] op_sel_hi:[1,0]
	v_pk_mul_f32 v[180:181], v[180:181], s[16:17] op_sel_hi:[1,0]
	v_pk_mul_f32 v[182:183], v[182:183], s[16:17] op_sel_hi:[1,0]
	v_pk_mul_f32 v[142:143], v[10:11], v[142:143]
	v_pk_mul_f32 v[144:145], v[6:7], v[144:145]
	v_pk_mul_f32 v[146:147], v[12:13], v[146:147]
	v_pk_mul_f32 v[148:149], v[8:9], v[148:149]
	v_pk_mul_f32 v[172:173], v[126:127], v[172:173]
	v_pk_mul_f32 v[178:179], v[130:131], v[178:179]
	v_pk_mul_f32 v[180:181], v[128:129], v[180:181]
	v_pk_mul_f32 v[182:183], v[132:133], v[182:183]
	v_cvt_pk_bf16_f32 v142, v142, v143
	v_cvt_pk_bf16_f32 v143, v146, v147
	v_cvt_pk_bf16_f32 v144, v144, v145
	v_cvt_pk_bf16_f32 v145, v148, v149
	v_cvt_pk_bf16_f32 v146, v172, v173
	v_cvt_pk_bf16_f32 v147, v180, v181
	v_cvt_pk_bf16_f32 v148, v178, v179
	v_cvt_pk_bf16_f32 v149, v182, v183
	global_store_dwordx4 v[170:171], v[142:145], off
	global_store_dwordx4 v[170:171], v[146:149], off offset:256
	s_nop 1
	s_branch .LBB0_1009
